# S4: S3 + K3 l1-loss hoisted under the main load batch (epilogue de-serialisation)
# speedup vs baseline: 1.0301x; 1.0145x over previous
_Z10epi_kernelPKDF16_PKfS2_S2_S2_S2_Pf:
	s_load_dwordx8 s[4:11], s[0:1], 0x0
	s_load_dwordx2 s[20:21], s[0:1], 0x20
	s_load_dwordx2 s[22:23], s[0:1], 0x30
	v_and_b32_e32 v55, 15, v0
	v_mov_b32_e32 v99, 0
	v_bfe_u32 v70, v0, 4, 2
	v_and_b32_e32 v2, 0xc0, v0
	v_lshl_or_b32 v16, v70, 3, v2
	v_lshlrev_b32_e32 v2, 10, v55
	v_mov_b32_e32 v3, v99
	v_lshrrev_b32_e32 v1, 6, v0
	s_waitcnt lgkmcnt(0)
	s_mov_b32 s30, 0
	v_readfirstlane_b32 s24, v1
	s_cmp_lg_u32 s2, 0xbf
	s_cbranch_scc1 .Lk3_l1skipB
	s_cmp_lg_u32 s24, 3
	s_cbranch_scc1 .Lk3_l1skipB
	s_mov_b32 s30, 1
	v_and_b32_e32 v124, 63, v0
	v_lshlrev_b32_e32 v124, 2, v124
	global_load_dword v112, v124, s[20:21]
	global_load_dword v113, v124, s[20:21] offset:256
	global_load_dword v114, v124, s[20:21] offset:512
	global_load_dword v115, v124, s[20:21] offset:768
	global_load_dword v116, v124, s[20:21] offset:1024
	global_load_dword v117, v124, s[20:21] offset:1280
	global_load_dword v118, v124, s[20:21] offset:1536
	global_load_dword v119, v124, s[20:21] offset:1792
	global_load_dword v120, v124, s[20:21] offset:2048
	global_load_dword v121, v124, s[20:21] offset:2304
	global_load_dword v122, v124, s[20:21] offset:2560
	global_load_dword v123, v124, s[20:21] offset:2816
.Lk3_l1skipB:
	v_lshl_add_u64 v[2:3], s[8:9], 0, v[2:3]
	v_lshlrev_b32_e32 v4, 2, v16
	v_mov_b32_e32 v5, v99
	s_bfe_i32 s16, s2, 0x1a0002
	v_lshl_add_u64 v[2:3], v[2:3], 0, v[4:5]
	v_lshlrev_b32_e32 v4, 2, v1
	s_mul_i32 s15, s16, 48
	v_lshl_add_u64 v[52:53], s[6:7], 0, v[4:5]
	s_mul_hi_i32 s6, s15, 0x4bda12f7
	s_lshr_b32 s7, s6, 31
	s_ashr_i32 s6, s6, 3
	s_add_i32 s6, s6, s7
	s_add_i32 s7, s15, 47
	s_mul_hi_i32 s7, s7, 0x4bda12f7
	s_lshr_b32 s8, s7, 31
	s_ashr_i32 s7, s7, 3
	s_lshl_b32 s3, s2, 4
	s_add_i32 s8, s7, s8
	s_and_b32 s14, s3, 48
	s_sub_i32 s7, s8, s6
	s_cmp_eq_u32 s7, 2
	s_mul_i32 s17, s6, 27
	s_cselect_b64 s[12:13], -1, 0
	s_lshl_b32 s9, s6, 1
	s_mul_hi_i32 s6, s17, 0x2aaaaaab
	s_lshr_b32 s7, s6, 31
	s_ashr_i32 s6, s6, 3
	s_add_i32 s6, s6, s7
	s_cmp_lg_u32 s6, s16
	s_cselect_b64 s[6:7], -1, 0
	s_add_i32 s17, s17, 27
	v_cndmask_b32_e64 v4, 0, 1, s[6:7]
	s_mul_hi_i32 s6, s17, 0x2aaaaaab
	s_lshr_b32 s7, s6, 31
	s_ashr_i32 s6, s6, 3
	s_add_i32 s6, s6, s7
	s_cmp_lg_u32 s6, s16
	s_cselect_b64 s[6:7], -1, 0
	v_cndmask_b32_e64 v6, 0, 1, s[6:7]
	v_or_b32_e32 v4, s9, v4
	v_or_b32_e32 v6, s9, v6
	s_lshl_b32 s9, s8, 1
	s_mul_i32 s8, s8, 27
	s_mul_hi_i32 s6, s8, 0x2aaaaaab
	s_lshr_b32 s7, s6, 31
	s_ashr_i32 s6, s6, 3
	s_add_i32 s6, s6, s7
	s_cmp_lg_u32 s6, s16
	s_cselect_b64 s[6:7], -1, 0
	v_cndmask_b32_e64 v8, 0, 1, s[6:7]
	v_ashrrev_i32_e32 v5, 31, v4
	v_add_u32_e32 v6, 2, v6
	v_or_b32_e32 v8, s9, v8
	global_load_dwordx4 v[18:21], v[2:3], off
	v_lshlrev_b64 v[4:5], 6, v[4:5]
	v_ashrrev_i32_e32 v7, 31, v6
	v_ashrrev_i32_e32 v9, 31, v8
	v_or_b32_e32 v4, v4, v55
	v_lshlrev_b64 v[6:7], 6, v[6:7]
	v_lshlrev_b64 v[8:9], 6, v[8:9]
	v_or_b32_e32 v4, s14, v4
	v_or_b32_e32 v6, v6, v55
	v_or_b32_e32 v8, v8, v55
	v_or_b32_e32 v6, s14, v6
	v_or_b32_e32 v8, s14, v8
	v_lshl_add_u64 v[10:11], v[4:5], 4, v[52:53]
	v_lshl_add_u64 v[12:13], v[6:7], 4, v[52:53]
	v_lshl_add_u64 v[14:15], v[8:9], 4, v[52:53]
	global_load_dword v71, v[10:11], off
	global_load_dword v72, v[12:13], off
	global_load_dword v73, v[14:15], off
	global_load_dwordx4 v[30:33], v[2:3], off offset:16
	global_load_dwordx4 v[26:29], v[2:3], off offset:128
	global_load_dwordx4 v[22:25], v[2:3], off offset:144
	v_lshlrev_b32_e32 v2, 1, v16
	v_mov_b32_e32 v3, v99
	v_lshl_add_u64 v[50:51], s[4:5], 0, v[2:3]
	v_lshlrev_b64 v[2:3], 9, v[4:5]
	v_lshl_add_u64 v[64:65], v[50:51], 0, v[2:3]
	v_lshlrev_b64 v[2:3], 9, v[6:7]
	v_lshl_add_u64 v[66:67], v[50:51], 0, v[2:3]
	v_lshlrev_b64 v[2:3], 9, v[8:9]
	global_load_dwordx4 v[34:37], v[64:65], off
	global_load_dwordx4 v[56:59], v[66:67], off
	v_lshl_add_u64 v[68:69], v[50:51], 0, v[2:3]
	global_load_dwordx4 v[60:63], v[68:69], off
	s_load_dwordx4 s[4:7], s[0:1], 0x20
	s_load_dwordx2 s[8:9], s[0:1], 0x30
	v_mul_u32_u24_e32 v2, 48, v55
	v_lshlrev_b32_e32 v98, 2, v55
	v_lshlrev_b32_e32 v106, 2, v2
	global_load_dword v100, v98, s[10:11]
	s_waitcnt lgkmcnt(0)
	global_load_dword v101, v98, s[6:7]
	global_load_dwordx4 v[2:5], v106, s[4:5] offset:48
	global_load_dwordx4 v[6:9], v106, s[4:5] offset:32
	global_load_dwordx4 v[10:13], v106, s[4:5] offset:16
	global_load_dwordx4 v[14:17], v106, s[4:5]
	global_load_dwordx4 v[46:49], v[64:65], off offset:64
	global_load_dwordx4 v[42:45], v[66:67], off offset:64
	global_load_dwordx4 v[38:41], v[68:69], off offset:64
	v_cndmask_b32_e64 v54, 0, 1.0, s[12:13]
	s_add_i32 s12, s16, 0x60
	s_add_i32 s16, s16, 48
	s_cmp_lg_u32 s30, 1
	s_cbranch_scc1 .Lk3_l1skipC
	s_mov_b64 s[28:29], vcc
	s_waitcnt vmcnt(19)
	v_add_f32_e64 v127, |v112|, |v113|
	v_add_f32_e64 v127, v127, |v114|
	v_add_f32_e64 v127, v127, |v115|
	v_add_f32_e64 v127, v127, |v116|
	v_add_f32_e64 v127, v127, |v117|
	v_add_f32_e64 v127, v127, |v118|
	v_add_f32_e64 v127, v127, |v119|
	v_add_f32_e64 v127, v127, |v120|
	v_add_f32_e64 v127, v127, |v121|
	v_add_f32_e64 v127, v127, |v122|
	v_add_f32_e64 v127, v127, |v123|
	v_xor_b32_e32 v125, 128, v124
	ds_bpermute_b32 v126, v125, v127
	s_waitcnt lgkmcnt(0)
	v_add_f32_e32 v127, v127, v126
	v_xor_b32_e32 v125, 64, v124
	ds_bpermute_b32 v126, v125, v127
	s_waitcnt lgkmcnt(0)
	v_add_f32_e32 v127, v127, v126
	v_xor_b32_e32 v125, 32, v124
	ds_bpermute_b32 v126, v125, v127
	s_waitcnt lgkmcnt(0)
	v_add_f32_e32 v127, v127, v126
	v_xor_b32_e32 v125, 16, v124
	ds_bpermute_b32 v126, v125, v127
	s_waitcnt lgkmcnt(0)
	v_add_f32_e32 v127, v127, v126
	v_xor_b32_e32 v125, 8, v124
	ds_bpermute_b32 v126, v125, v127
	s_waitcnt lgkmcnt(0)
	v_add_f32_e32 v127, v127, v126
	v_xor_b32_e32 v125, 4, v124
	ds_bpermute_b32 v126, v125, v127
	s_waitcnt lgkmcnt(0)
	v_add_f32_e32 v127, v127, v126
	s_mov_b32 s25, 0x44400000
	v_div_scale_f32 v125, s[26:27], s25, s25, v127
	v_rcp_f32_e32 v126, v125
	s_nop 0
	v_fma_f32 v123, -v125, v126, 1.0
	v_fmac_f32_e32 v126, v123, v126
	v_div_scale_f32 v123, vcc, v127, s25, v127
	v_mul_f32_e32 v122, v123, v126
	v_fma_f32 v121, -v125, v122, v123
	v_fmac_f32_e32 v122, v121, v126
	v_fma_f32 v125, -v125, v122, v123
	s_nop 3
	v_div_fmas_f32 v125, v125, v126, v122
	v_div_fixup_f32 v127, v125, s25, v127
	v_mov_b32_e32 v125, 0x30000
	v_cmp_eq_u32_e32 vcc, 0, v124
	s_and_saveexec_b64 s[26:27], vcc
	global_store_dword v125, v127, s[22:23]
	s_mov_b64 exec, s[26:27]
	s_mov_b64 vcc, s[28:29]
.Lk3_l1skipC:
	s_waitcnt vmcnt(18)
	v_cvt_f16_f32_e32 v104, v18
	s_waitcnt vmcnt(16)
	v_add_f32_e32 v18, v71, v72
	s_waitcnt vmcnt(15)
	v_fmac_f32_e32 v18, v54, v73
	v_div_scale_f32 v64, s[0:1], v18, v18, 1.0
	v_rcp_f32_e32 v65, v64
	s_waitcnt vmcnt(14)
	v_cvt_f16_f32_e32 v105, v33
	s_add_i32 s1, s15, 0x1200
	s_add_i32 s0, s15, 0x900
	v_fma_f32 v33, -v64, v65, 1.0
	v_fmac_f32_e32 v65, v33, v65
	v_div_scale_f32 v33, vcc, 1.0, v18, 1.0
	v_mul_f32_e32 v66, v33, v65
	v_fma_f32 v67, -v64, v66, v33
	v_fmac_f32_e32 v66, v67, v65
	v_fma_f32 v33, -v64, v66, v33
	v_div_fmas_f32 v33, v33, v65, v66
	s_waitcnt vmcnt(11)
	v_cvt_f32_f16_e32 v64, v34
	v_cvt_f32_f16_sdwa v65, v34 dst_sel:DWORD dst_unused:UNUSED_PAD src0_sel:WORD_1
	s_waitcnt vmcnt(10)
	v_cvt_f32_f16_e32 v66, v56
	v_cvt_f32_f16_sdwa v67, v56 dst_sel:DWORD dst_unused:UNUSED_PAD src0_sel:WORD_1
	s_waitcnt vmcnt(9)
	v_cvt_f32_f16_e32 v68, v60
	v_cvt_f32_f16_sdwa v69, v60 dst_sel:DWORD dst_unused:UNUSED_PAD src0_sel:WORD_1
	v_div_fixup_f32 v33, v33, v18, 1.0
	v_cmp_lt_f32_e32 vcc, 0, v18
	v_pk_add_f32 v[64:65], v[64:65], v[66:67]
	v_mul_u32_u24_e32 v34, 0x110, v70
	v_cndmask_b32_e32 v18, 0, v33, vcc
	v_pk_fma_f32 v[64:65], v[54:55], v[68:69], v[64:65] op_sel_hi:[0,1,1]
	v_pk_mul_f32 v[64:65], v[18:19], v[64:65] op_sel_hi:[0,1]
	v_mul_f32_e32 v33, 0x3fb8aa3b, v64
	v_exp_f32_e32 v66, v33
	v_mul_f32_e32 v33, 0x3fb8aa3b, v65
	v_exp_f32_e32 v67, v33
	v_mul_u32_u24_e32 v33, 0x440, v1
	v_add3_u32 v33, v33, v34, v98
	v_cvt_f32_f16_e32 v34, v35
	v_cvt_f32_f16_sdwa v35, v35 dst_sel:DWORD dst_unused:UNUSED_PAD src0_sel:WORD_1
	v_cvt_f32_f16_e32 v56, v57
	v_cvt_f32_f16_sdwa v57, v57 dst_sel:DWORD dst_unused:UNUSED_PAD src0_sel:WORD_1
	v_cvt_f32_f16_e32 v60, v61
	v_cvt_f32_f16_sdwa v61, v61 dst_sel:DWORD dst_unused:UNUSED_PAD src0_sel:WORD_1
	v_pk_add_f32 v[66:67], v[66:67], -1.0 op_sel_hi:[1,0]
	v_pk_add_f32 v[34:35], v[34:35], v[56:57]
	v_cmp_lt_f32_e32 vcc, 0, v65
	v_pk_fma_f32 v[34:35], v[54:55], v[60:61], v[34:35] op_sel_hi:[0,1,1]
	v_pk_mul_f32 v[56:57], v[18:19], v[34:35] op_sel_hi:[0,1]
	v_mul_f32_e32 v34, 0x3fb8aa3b, v56
	v_cndmask_b32_e32 v65, v67, v65, vcc
	v_exp_f32_e32 v60, v34
	v_mul_f32_e32 v34, 0x3fb8aa3b, v57
	v_cmp_lt_f32_e32 vcc, 0, v64
	v_exp_f32_e32 v61, v34
	v_cvt_f32_f16_sdwa v67, v58 dst_sel:DWORD dst_unused:UNUSED_PAD src0_sel:WORD_1
	v_cndmask_b32_e32 v34, v66, v64, vcc
	v_cvt_pk_f16_f32 v34, v34, v65
	v_cvt_f32_f16_e32 v64, v36
	v_cvt_f32_f16_sdwa v65, v36 dst_sel:DWORD dst_unused:UNUSED_PAD src0_sel:WORD_1
	v_cvt_f32_f16_e32 v66, v58
	v_cvt_f32_f16_e32 v68, v62
	v_cvt_f32_f16_sdwa v69, v62 dst_sel:DWORD dst_unused:UNUSED_PAD src0_sel:WORD_1
	v_pk_add_f32 v[60:61], v[60:61], -1.0 op_sel_hi:[1,0]
	v_pk_add_f32 v[64:65], v[64:65], v[66:67]
	v_cmp_lt_f32_e32 vcc, 0, v57
	v_pk_fma_f32 v[64:65], v[54:55], v[68:69], v[64:65] op_sel_hi:[0,1,1]
	v_pk_mul_f32 v[64:65], v[18:19], v[64:65] op_sel_hi:[0,1]
	v_mul_f32_e32 v36, 0x3fb8aa3b, v64
	v_cndmask_b32_e32 v35, v61, v57, vcc
	v_exp_f32_e32 v66, v36
	v_mul_f32_e32 v36, 0x3fb8aa3b, v65
	v_cmp_lt_f32_e32 vcc, 0, v56
	v_exp_f32_e32 v67, v36
	v_cvt_f32_f16_e32 v58, v59
	v_cndmask_b32_e32 v36, v60, v56, vcc
	v_cvt_pk_f16_f32 v35, v36, v35
	v_cvt_f32_f16_e32 v36, v37
	v_cvt_f32_f16_sdwa v37, v37 dst_sel:DWORD dst_unused:UNUSED_PAD src0_sel:WORD_1
	v_cvt_f32_f16_sdwa v59, v59 dst_sel:DWORD dst_unused:UNUSED_PAD src0_sel:WORD_1
	v_cvt_f32_f16_e32 v60, v63
	v_cvt_f32_f16_sdwa v61, v63 dst_sel:DWORD dst_unused:UNUSED_PAD src0_sel:WORD_1
	v_pk_add_f32 v[56:57], v[66:67], -1.0 op_sel_hi:[1,0]
	v_pk_add_f32 v[36:37], v[36:37], v[58:59]
	v_cmp_lt_f32_e32 vcc, 0, v65
	v_pk_fma_f32 v[36:37], v[54:55], v[60:61], v[36:37] op_sel_hi:[0,1,1]
	v_pk_mul_f32 v[58:59], v[18:19], v[36:37] op_sel_hi:[0,1]
	v_mul_f32_e32 v36, 0x3fb8aa3b, v58
	v_cndmask_b32_e32 v57, v57, v65, vcc
	v_exp_f32_e32 v60, v36
	v_mul_f32_e32 v36, 0x3fb8aa3b, v59
	v_cmp_lt_f32_e32 vcc, 0, v64
	v_exp_f32_e32 v61, v36
	s_waitcnt vmcnt(1)
	v_cvt_f32_f16_e32 v62, v42
	v_cndmask_b32_e32 v36, v56, v64, vcc
	v_cvt_pk_f16_f32 v36, v36, v57
	v_cvt_f32_f16_e32 v56, v46
	v_cvt_f32_f16_sdwa v57, v46 dst_sel:DWORD dst_unused:UNUSED_PAD src0_sel:WORD_1
	v_cvt_f32_f16_sdwa v63, v42 dst_sel:DWORD dst_unused:UNUSED_PAD src0_sel:WORD_1
	s_mul_hi_i32 s1, s1, 0x4bda12f7
	s_waitcnt vmcnt(0)
	v_cvt_f32_f16_e32 v64, v38
	v_cvt_f32_f16_sdwa v65, v38 dst_sel:DWORD dst_unused:UNUSED_PAD src0_sel:WORD_1
	s_lshr_b32 s6, s1, 31
	s_ashr_i32 s1, s1, 3
	s_mul_hi_i32 s0, s0, 0x4bda12f7
	s_add_i32 s10, s1, s6
	s_lshr_b32 s1, s0, 31
	s_ashr_i32 s0, s0, 3
	s_add_i32 s6, s0, s1
	v_pk_add_f32 v[56:57], v[56:57], v[62:63]
	s_mul_i32 s11, s6, 27
	v_pk_fma_f32 v[56:57], v[54:55], v[64:65], v[56:57] op_sel_hi:[0,1,1]
	s_mul_hi_i32 s0, s11, 0x2aaaaaab
	v_pk_mul_f32 v[56:57], v[18:19], v[56:57] op_sel_hi:[0,1]
	s_lshr_b32 s1, s0, 31
	s_ashr_i32 s0, s0, 3
	v_pk_add_f32 v[60:61], v[60:61], -1.0 op_sel_hi:[1,0]
	v_cmp_lt_f32_e32 vcc, 0, v59
	v_mul_f32_e32 v38, 0x3fb8aa3b, v56
	s_lshl_b32 s7, s6, 1
	s_add_i32 s0, s0, s1
	v_cndmask_b32_e32 v37, v61, v59, vcc
	v_exp_f32_e32 v62, v38
	v_mul_f32_e32 v38, 0x3fb8aa3b, v57
	v_cmp_lt_f32_e32 vcc, 0, v58
	s_cmp_lg_u32 s0, s16
	v_exp_f32_e32 v63, v38
	v_cndmask_b32_e32 v38, v60, v58, vcc
	s_cselect_b64 s[0:1], -1, 0
	s_add_i32 s11, s11, 27
	v_cvt_pk_f16_f32 v37, v38, v37
	v_cndmask_b32_e64 v38, 0, 1, s[0:1]
	s_mul_hi_i32 s0, s11, 0x2aaaaaab
	v_or_b32_e32 v60, s7, v38
	s_lshr_b32 s1, s0, 31
	s_ashr_i32 s0, s0, 3
	v_ashrrev_i32_e32 v61, 31, v60
	s_add_i32 s0, s0, s1
	v_lshlrev_b64 v[60:61], 6, v[60:61]
	s_cmp_lg_u32 s0, s16
	v_or_b32_e32 v38, v60, v55
	s_cselect_b64 s[0:1], -1, 0
	v_or_b32_e32 v60, s14, v38
	v_cndmask_b32_e64 v38, 0, 1, s[0:1]
	s_add_i32 s0, s15, 0x92f
	s_addk_i32 s15, 0x122f
	s_mul_hi_i32 s1, s15, 0x4bda12f7
	v_or_b32_e32 v38, s7, v38
	s_lshr_b32 s7, s1, 31
	s_ashr_i32 s1, s1, 3
	s_mul_hi_i32 s0, s0, 0x4bda12f7
	s_add_i32 s13, s1, s7
	s_lshr_b32 s1, s0, 31
	s_ashr_i32 s0, s0, 3
	s_add_i32 s7, s0, s1
	s_mul_i32 s0, s7, 27
	s_mul_hi_i32 s0, s0, 0x2aaaaaab
	v_pk_add_f32 v[58:59], v[62:63], -1.0 op_sel_hi:[1,0]
	v_add_u32_e32 v62, 2, v38
	s_lshr_b32 s1, s0, 31
	s_ashr_i32 s0, s0, 3
	v_ashrrev_i32_e32 v63, 31, v62
	s_lshl_b32 s11, s7, 1
	s_add_i32 s0, s0, s1
	v_lshlrev_b64 v[62:63], 6, v[62:63]
	s_cmp_lg_u32 s0, s16
	v_or_b32_e32 v38, v62, v55
	s_cselect_b64 s[0:1], -1, 0
	v_or_b32_e32 v62, s14, v38
	v_cndmask_b32_e64 v38, 0, 1, s[0:1]
	s_sub_i32 s6, s7, s6
	s_sub_i32 s0, s13, s10
	s_cmp_eq_u32 s0, 2
	s_cselect_b64 s[0:1], -1, 0
	s_cmp_eq_u32 s6, 2
	s_mul_i32 s16, s10, 27
	s_cselect_b64 s[6:7], -1, 0
	s_lshl_b32 s15, s10, 1
	s_mul_hi_i32 s10, s16, 0x2aaaaaab
	v_or_b32_e32 v64, s11, v38
	s_lshr_b32 s11, s10, 31
	s_ashr_i32 s10, s10, 3
	v_ashrrev_i32_e32 v65, 31, v64
	s_add_i32 s10, s10, s11
	v_lshlrev_b64 v[64:65], 6, v[64:65]
	s_cmp_lg_u32 s10, s12
	v_or_b32_e32 v38, v64, v55
	s_cselect_b64 s[10:11], -1, 0
	s_add_i32 s16, s16, 27
	v_or_b32_e32 v64, s14, v38
	v_lshl_add_u64 v[66:67], v[60:61], 4, v[52:53]
	v_cndmask_b32_e64 v38, 0, 1, s[10:11]
	s_mul_hi_i32 s10, s16, 0x2aaaaaab
	v_lshl_add_u64 v[68:69], v[62:63], 4, v[52:53]
	v_lshl_add_u64 v[70:71], v[64:65], 4, v[52:53]
	global_load_dword v73, v[66:67], off
	global_load_dword v83, v[68:69], off
	global_load_dword v97, v[70:71], off
	v_or_b32_e32 v66, s15, v38
	s_lshr_b32 s11, s10, 31
	s_ashr_i32 s10, s10, 3
	v_ashrrev_i32_e32 v67, 31, v66
	s_add_i32 s10, s10, s11
	v_lshlrev_b64 v[70:71], 6, v[66:67]
	s_cmp_lg_u32 s10, s12
	v_or_b32_e32 v38, v70, v55
	s_cselect_b64 s[10:11], -1, 0
	v_or_b32_e32 v70, s14, v38
	v_cndmask_b32_e64 v38, 0, 1, s[10:11]
	v_or_b32_e32 v38, s15, v38
	s_lshl_b32 s15, s13, 1
	s_mul_i32 s13, s13, 27
	s_mul_hi_i32 s10, s13, 0x2aaaaaab
	v_add_u32_e32 v66, 2, v38
	s_lshr_b32 s11, s10, 31
	s_ashr_i32 s10, s10, 3
	v_ashrrev_i32_e32 v67, 31, v66
	s_add_i32 s10, s10, s11
	v_lshlrev_b64 v[102:103], 6, v[66:67]
	s_cmp_lg_u32 s10, s12
	v_or_b32_e32 v38, v102, v55
	s_cselect_b64 s[10:11], -1, 0
	v_or_b32_e32 v102, s14, v38
	v_cndmask_b32_e64 v38, 0, 1, s[10:11]
	v_or_b32_e32 v66, s15, v38
	v_ashrrev_i32_e32 v67, 31, v66
	v_lshlrev_b64 v[108:109], 6, v[66:67]
	v_or_b32_e32 v38, v108, v55
	v_or_b32_e32 v108, s14, v38
	v_lshl_add_u64 v[66:67], v[70:71], 4, v[52:53]
	v_lshl_add_u64 v[68:69], v[102:103], 4, v[52:53]
	v_lshl_add_u64 v[52:53], v[108:109], 4, v[52:53]
	global_load_dword v72, v[66:67], off
	global_load_dword v82, v[68:69], off
	global_load_dword v96, v[52:53], off
	v_cvt_f32_f16_e32 v46, v47
	v_cvt_f32_f16_sdwa v47, v47 dst_sel:DWORD dst_unused:UNUSED_PAD src0_sel:WORD_1
	v_cvt_f32_f16_e32 v42, v43
	v_cvt_f32_f16_sdwa v43, v43 dst_sel:DWORD dst_unused:UNUSED_PAD src0_sel:WORD_1
	v_cvt_f32_f16_e32 v38, v39
	v_cvt_f32_f16_sdwa v39, v39 dst_sel:DWORD dst_unused:UNUSED_PAD src0_sel:WORD_1
	v_cmp_lt_f32_e32 vcc, 0, v57
	v_pk_add_f32 v[42:43], v[46:47], v[42:43]
	v_cvt_f16_f32_e32 v26, v26
	v_cndmask_b32_e32 v55, v59, v57, vcc
	v_pk_fma_f32 v[38:39], v[54:55], v[38:39], v[42:43] op_sel_hi:[0,1,1]
	v_pk_mul_f32 v[42:43], v[18:19], v[38:39] op_sel_hi:[0,1]
	v_mul_f32_e32 v38, 0x3fb8aa3b, v42
	v_exp_f32_e32 v46, v38
	v_mul_f32_e32 v38, 0x3fb8aa3b, v43
	v_exp_f32_e32 v47, v38
	v_lshlrev_b64 v[38:39], 9, v[60:61]
	v_lshl_add_u64 v[52:53], v[50:51], 0, v[38:39]
	v_lshlrev_b64 v[38:39], 9, v[62:63]
	v_lshl_add_u64 v[60:61], v[50:51], 0, v[38:39]
	v_lshlrev_b64 v[38:39], 9, v[64:65]
	global_load_dwordx4 v[84:87], v[52:53], off
	v_lshl_add_u64 v[62:63], v[50:51], 0, v[38:39]
	global_load_dwordx4 v[88:91], v[60:61], off
	global_load_dwordx4 v[92:95], v[62:63], off
	global_load_dwordx4 v[78:81], v[52:53], off offset:64
	global_load_dwordx4 v[74:77], v[60:61], off offset:64
	global_load_dwordx4 v[66:69], v[62:63], off offset:64
	v_cmp_lt_f32_e32 vcc, 0, v56
	v_cvt_f32_f16_sdwa v57, v48 dst_sel:DWORD dst_unused:UNUSED_PAD src0_sel:WORD_1
	v_cvt_f32_f16_sdwa v59, v44 dst_sel:DWORD dst_unused:UNUSED_PAD src0_sel:WORD_1
	v_cndmask_b32_e32 v38, v58, v56, vcc
	v_cvt_f32_f16_e32 v56, v48
	v_cvt_f32_f16_e32 v58, v44
	v_cvt_f32_f16_e32 v64, v40
	v_cvt_f32_f16_sdwa v65, v40 dst_sel:DWORD dst_unused:UNUSED_PAD src0_sel:WORD_1
	v_pk_add_f32 v[46:47], v[46:47], -1.0 op_sel_hi:[1,0]
	v_pk_add_f32 v[56:57], v[56:57], v[58:59]
	v_cmp_lt_f32_e32 vcc, 0, v43
	v_pk_fma_f32 v[56:57], v[54:55], v[64:65], v[56:57] op_sel_hi:[0,1,1]
	v_pk_mul_f32 v[56:57], v[18:19], v[56:57] op_sel_hi:[0,1]
	v_mul_f32_e32 v40, 0x3fb8aa3b, v56
	v_cndmask_b32_e32 v39, v47, v43, vcc
	v_exp_f32_e32 v58, v40
	v_mul_f32_e32 v40, 0x3fb8aa3b, v57
	v_cmp_lt_f32_e32 vcc, 0, v42
	v_exp_f32_e32 v59, v40
	v_cvt_f32_f16_sdwa v47, v49 dst_sel:DWORD dst_unused:UNUSED_PAD src0_sel:WORD_1
	v_cndmask_b32_e32 v40, v46, v42, vcc
	v_cvt_f32_f16_e32 v46, v49
	v_cvt_f32_f16_e32 v44, v45
	v_cvt_f32_f16_sdwa v45, v45 dst_sel:DWORD dst_unused:UNUSED_PAD src0_sel:WORD_1
	v_cvt_pk_f16_f32 v39, v40, v39
	v_cvt_f32_f16_e32 v40, v41
	v_cvt_f32_f16_sdwa v41, v41 dst_sel:DWORD dst_unused:UNUSED_PAD src0_sel:WORD_1
	v_pk_add_f32 v[44:45], v[46:47], v[44:45]
	v_pk_add_f32 v[42:43], v[58:59], -1.0 op_sel_hi:[1,0]
	v_cmp_lt_f32_e32 vcc, 0, v57
	v_pk_fma_f32 v[40:41], v[54:55], v[40:41], v[44:45] op_sel_hi:[0,1,1]
	v_pk_mul_f32 v[44:45], v[18:19], v[40:41] op_sel_hi:[0,1]
	v_mul_f32_e32 v18, 0x3fb8aa3b, v44
	v_exp_f32_e32 v46, v18
	v_mul_f32_e32 v18, 0x3fb8aa3b, v45
	v_exp_f32_e32 v47, v18
	v_cndmask_b32_e32 v43, v43, v57, vcc
	v_cmp_lt_f32_e32 vcc, 0, v56
	v_cvt_pk_f16_f32 v38, v38, v55
	v_cvt_f16_f32_e32 v25, v25
	v_cndmask_b32_e32 v18, v42, v56, vcc
	v_cvt_pk_f16_f32 v40, v18, v43
	v_pk_add_f32 v[42:43], v[46:47], -1.0 op_sel_hi:[1,0]
	v_cmp_lt_f32_e32 vcc, 0, v45
	s_waitcnt vmcnt(3)
	v_cvt_f32_f16_sdwa v53, v92 dst_sel:DWORD dst_unused:UNUSED_PAD src0_sel:WORD_1
	v_cndmask_b32_e32 v18, v43, v45, vcc
	v_cmp_lt_f32_e32 vcc, 0, v44
	s_nop 1
	v_cndmask_b32_e32 v41, v42, v44, vcc
	v_lshlrev_b64 v[42:43], 9, v[70:71]
	v_lshl_add_u64 v[46:47], v[50:51], 0, v[42:43]
	v_lshlrev_b64 v[42:43], 9, v[102:103]
	v_cndmask_b32_e64 v103, 0, 1.0, s[6:7]
	v_cndmask_b32_e64 v102, 0, 1.0, s[0:1]
	v_pk_add_f32 v[44:45], v[72:73], v[82:83]
	v_cvt_pk_f16_f32 v41, v41, v18
	v_pk_fma_f32 v[82:83], v[102:103], v[96:97], v[44:45]
	v_lshl_add_u64 v[48:49], v[50:51], 0, v[42:43]
	v_div_scale_f32 v18, s[0:1], v83, v83, 1.0
	v_rcp_f32_e32 v52, v18
	v_lshlrev_b64 v[42:43], 9, v[108:109]
	v_lshl_add_u64 v[96:97], v[50:51], 0, v[42:43]
	global_load_dwordx4 v[58:61], v[46:47], off
	global_load_dwordx4 v[42:45], v[46:47], off offset:64
	v_fma_f32 v46, -v18, v52, 1.0
	v_fmac_f32_e32 v52, v46, v52
	v_div_scale_f32 v46, vcc, 1.0, v83, 1.0
	v_mul_f32_e32 v47, v46, v52
	v_fma_f32 v50, -v18, v47, v46
	v_fmac_f32_e32 v47, v50, v52
	v_fma_f32 v18, -v18, v47, v46
	v_div_fmas_f32 v18, v18, v52, v47
	v_cvt_f32_f16_e32 v46, v84
	v_cvt_f32_f16_sdwa v47, v84 dst_sel:DWORD dst_unused:UNUSED_PAD src0_sel:WORD_1
	v_cvt_f32_f16_e32 v50, v88
	v_cvt_f32_f16_sdwa v51, v88 dst_sel:DWORD dst_unused:UNUSED_PAD src0_sel:WORD_1
	v_cvt_f32_f16_e32 v52, v92
	v_div_fixup_f32 v18, v18, v83, 1.0
	v_cmp_lt_f32_e32 vcc, 0, v83
	v_pk_add_f32 v[46:47], v[46:47], v[50:51]
	v_mov_b32_e32 v84, v103
	v_cndmask_b32_e32 v18, 0, v18, vcc
	v_pk_fma_f32 v[46:47], v[84:85], v[52:53], v[46:47] op_sel_hi:[0,1,1]
	v_pk_mul_f32 v[46:47], v[18:19], v[46:47] op_sel_hi:[0,1]
	v_mul_f32_e32 v50, 0x3fb8aa3b, v46
	v_exp_f32_e32 v108, v50
	v_mul_f32_e32 v50, 0x3fb8aa3b, v47
	v_exp_f32_e32 v109, v50
	global_load_dwordx4 v[70:73], v[48:49], off
	global_load_dwordx4 v[50:53], v[48:49], off offset:64
	global_load_dwordx4 v[62:65], v[96:97], off
	global_load_dwordx4 v[54:57], v[96:97], off offset:64
	v_cvt_f32_f16_e32 v96, v85
	v_cvt_f32_f16_sdwa v97, v85 dst_sel:DWORD dst_unused:UNUSED_PAD src0_sel:WORD_1
	v_cvt_f32_f16_e32 v88, v89
	v_cvt_f32_f16_sdwa v89, v89 dst_sel:DWORD dst_unused:UNUSED_PAD src0_sel:WORD_1
	v_cvt_f32_f16_e32 v92, v93
	v_cvt_f32_f16_sdwa v93, v93 dst_sel:DWORD dst_unused:UNUSED_PAD src0_sel:WORD_1
	v_pk_add_f32 v[48:49], v[108:109], -1.0 op_sel_hi:[1,0]
	v_pk_add_f32 v[88:89], v[96:97], v[88:89]
	v_cmp_lt_f32_e32 vcc, 0, v47
	v_pk_fma_f32 v[88:89], v[84:85], v[92:93], v[88:89] op_sel_hi:[0,1,1]
	v_pk_mul_f32 v[88:89], v[18:19], v[88:89] op_sel_hi:[0,1]
	v_cndmask_b32_e32 v47, v49, v47, vcc
	v_mul_f32_e32 v49, 0x3fb8aa3b, v88
	v_exp_f32_e32 v92, v49
	v_mul_f32_e32 v49, 0x3fb8aa3b, v89
	v_exp_f32_e32 v93, v49
	v_cmp_lt_f32_e32 vcc, 0, v46
	v_cvt_f32_f16_e32 v96, v90
	v_cvt_f32_f16_sdwa v97, v90 dst_sel:DWORD dst_unused:UNUSED_PAD src0_sel:WORD_1
	v_cndmask_b32_e32 v46, v48, v46, vcc
	v_pk_add_f32 v[48:49], v[92:93], -1.0 op_sel_hi:[1,0]
	v_cvt_f32_f16_e32 v92, v86
	v_cvt_f32_f16_sdwa v93, v86 dst_sel:DWORD dst_unused:UNUSED_PAD src0_sel:WORD_1
	v_cvt_f32_f16_e32 v108, v94
	v_cvt_f32_f16_sdwa v109, v94 dst_sel:DWORD dst_unused:UNUSED_PAD src0_sel:WORD_1
	v_cmp_lt_f32_e32 vcc, 0, v89
	v_pk_add_f32 v[92:93], v[92:93], v[96:97]
	v_cvt_pk_f16_f32 v46, v46, v47
	v_pk_fma_f32 v[92:93], v[84:85], v[108:109], v[92:93] op_sel_hi:[0,1,1]
	v_pk_mul_f32 v[92:93], v[18:19], v[92:93] op_sel_hi:[0,1]
	v_cndmask_b32_e32 v47, v49, v89, vcc
	v_mul_f32_e32 v49, 0x3fb8aa3b, v92
	v_exp_f32_e32 v96, v49
	v_mul_f32_e32 v49, 0x3fb8aa3b, v93
	v_cmp_lt_f32_e32 vcc, 0, v88
	v_exp_f32_e32 v97, v49
	v_cvt_f32_f16_e32 v86, v87
	v_cndmask_b32_e32 v48, v48, v88, vcc
	v_cvt_f32_f16_sdwa v87, v87 dst_sel:DWORD dst_unused:UNUSED_PAD src0_sel:WORD_1
	v_cvt_f32_f16_e32 v88, v91
	v_cvt_f32_f16_sdwa v89, v91 dst_sel:DWORD dst_unused:UNUSED_PAD src0_sel:WORD_1
	v_cvt_f32_f16_e32 v90, v95
	v_cvt_f32_f16_sdwa v91, v95 dst_sel:DWORD dst_unused:UNUSED_PAD src0_sel:WORD_1
	v_cvt_pk_f16_f32 v47, v48, v47
	v_pk_add_f32 v[48:49], v[96:97], -1.0 op_sel_hi:[1,0]
	v_cmp_lt_f32_e32 vcc, 0, v93
	v_pk_add_f32 v[86:87], v[86:87], v[88:89]
	s_waitcnt vmcnt(6)
	v_cvt_f32_f16_e32 v94, v66
	v_cndmask_b32_e32 v49, v49, v93, vcc
	v_pk_fma_f32 v[86:87], v[84:85], v[90:91], v[86:87] op_sel_hi:[0,1,1]
	v_cmp_lt_f32_e32 vcc, 0, v92
	v_pk_mul_f32 v[86:87], v[18:19], v[86:87] op_sel_hi:[0,1]
	v_cvt_f32_f16_e32 v90, v78
	v_cndmask_b32_e32 v48, v48, v92, vcc
	v_cvt_f32_f16_sdwa v91, v78 dst_sel:DWORD dst_unused:UNUSED_PAD src0_sel:WORD_1
	v_cvt_f32_f16_e32 v92, v74
	v_cvt_f32_f16_sdwa v93, v74 dst_sel:DWORD dst_unused:UNUSED_PAD src0_sel:WORD_1
	v_mul_f32_e32 v83, 0x3fb8aa3b, v86
	v_cvt_f32_f16_sdwa v95, v66 dst_sel:DWORD dst_unused:UNUSED_PAD src0_sel:WORD_1
	v_exp_f32_e32 v88, v83
	v_mul_f32_e32 v83, 0x3fb8aa3b, v87
	v_exp_f32_e32 v89, v83
	v_pk_add_f32 v[90:91], v[90:91], v[92:93]
	v_cmp_lt_f32_e32 vcc, 0, v87
	v_pk_fma_f32 v[90:91], v[84:85], v[94:95], v[90:91] op_sel_hi:[0,1,1]
	v_pk_mul_f32 v[90:91], v[18:19], v[90:91] op_sel_hi:[0,1]
	v_pk_add_f32 v[88:89], v[88:89], -1.0 op_sel_hi:[1,0]
	v_mul_f32_e32 v66, 0x3fb8aa3b, v90
	v_cvt_pk_f16_f32 v48, v48, v49
	v_cndmask_b32_e32 v49, v89, v87, vcc
	v_exp_f32_e32 v92, v66
	v_mul_f32_e32 v66, 0x3fb8aa3b, v91
	v_cmp_lt_f32_e32 vcc, 0, v86
	v_exp_f32_e32 v93, v66
	v_cvt_f32_f16_e32 v78, v79
	v_cndmask_b32_e32 v66, v88, v86, vcc
	v_cvt_f32_f16_sdwa v79, v79 dst_sel:DWORD dst_unused:UNUSED_PAD src0_sel:WORD_1
	v_cvt_f32_f16_e32 v74, v75
	v_cvt_f32_f16_sdwa v75, v75 dst_sel:DWORD dst_unused:UNUSED_PAD src0_sel:WORD_1
	v_cvt_pk_f16_f32 v49, v66, v49
	v_cvt_f32_f16_e32 v66, v67
	v_cvt_f32_f16_sdwa v67, v67 dst_sel:DWORD dst_unused:UNUSED_PAD src0_sel:WORD_1
	v_pk_add_f32 v[74:75], v[78:79], v[74:75]
	v_pk_add_f32 v[86:87], v[92:93], -1.0 op_sel_hi:[1,0]
	v_cmp_lt_f32_e32 vcc, 0, v91
	v_pk_fma_f32 v[66:67], v[84:85], v[66:67], v[74:75] op_sel_hi:[0,1,1]
	v_pk_mul_f32 v[74:75], v[18:19], v[66:67] op_sel_hi:[0,1]
	v_mul_f32_e32 v66, 0x3fb8aa3b, v74
	v_cndmask_b32_e32 v83, v87, v91, vcc
	v_exp_f32_e32 v78, v66
	v_mul_f32_e32 v66, 0x3fb8aa3b, v75
	v_cmp_lt_f32_e32 vcc, 0, v90
	v_exp_f32_e32 v79, v66
	v_cvt_f32_f16_sdwa v87, v80 dst_sel:DWORD dst_unused:UNUSED_PAD src0_sel:WORD_1
	v_cndmask_b32_e32 v66, v86, v90, vcc
	v_cvt_f32_f16_e32 v86, v80
	v_cvt_f32_f16_e32 v88, v76
	v_cvt_f32_f16_sdwa v89, v76 dst_sel:DWORD dst_unused:UNUSED_PAD src0_sel:WORD_1
	v_cvt_f32_f16_e32 v90, v68
	v_cvt_f32_f16_sdwa v91, v68 dst_sel:DWORD dst_unused:UNUSED_PAD src0_sel:WORD_1
	v_pk_add_f32 v[78:79], v[78:79], -1.0 op_sel_hi:[1,0]
	v_pk_add_f32 v[86:87], v[86:87], v[88:89]
	v_cmp_lt_f32_e32 vcc, 0, v75
	v_pk_fma_f32 v[86:87], v[84:85], v[90:91], v[86:87] op_sel_hi:[0,1,1]
	v_pk_mul_f32 v[86:87], v[18:19], v[86:87] op_sel_hi:[0,1]
	v_mul_f32_e32 v68, 0x3fb8aa3b, v86
	v_exp_f32_e32 v88, v68
	v_mul_f32_e32 v68, 0x3fb8aa3b, v87
	v_exp_f32_e32 v89, v68
	v_cndmask_b32_e32 v67, v79, v75, vcc
	v_cmp_lt_f32_e32 vcc, 0, v74
	v_cvt_f32_f16_sdwa v79, v81 dst_sel:DWORD dst_unused:UNUSED_PAD src0_sel:WORD_1
	v_cvt_f32_f16_e32 v76, v77
	v_cndmask_b32_e32 v68, v78, v74, vcc
	v_cvt_f32_f16_e32 v78, v81
	v_cvt_f32_f16_sdwa v77, v77 dst_sel:DWORD dst_unused:UNUSED_PAD src0_sel:WORD_1
	v_cvt_f32_f16_e32 v80, v69
	v_cvt_f32_f16_sdwa v81, v69 dst_sel:DWORD dst_unused:UNUSED_PAD src0_sel:WORD_1
	v_pk_add_f32 v[74:75], v[88:89], -1.0 op_sel_hi:[1,0]
	v_cmp_lt_f32_e32 vcc, 0, v87
	v_cvt_pk_f16_f32 v67, v68, v67
	v_cvt_pk_f16_f32 v66, v66, v83
	v_cndmask_b32_e32 v68, v75, v87, vcc
	v_cmp_lt_f32_e32 vcc, 0, v86
	s_waitcnt vmcnt(2)
	v_cvt_f32_f16_sdwa v107, v52 dst_sel:DWORD dst_unused:UNUSED_PAD src0_sel:WORD_1
	v_cndmask_b32_e32 v69, v74, v86, vcc
	v_pk_add_f32 v[74:75], v[78:79], v[76:77]
	v_cvt_pk_f16_f32 v68, v69, v68
	v_pk_fma_f32 v[74:75], v[84:85], v[80:81], v[74:75] op_sel_hi:[0,1,1]
	v_pk_mul_f32 v[74:75], v[18:19], v[74:75] op_sel_hi:[0,1]
	v_mul_f32_e32 v18, 0x3fb8aa3b, v74
	v_exp_f32_e32 v76, v18
	v_mul_f32_e32 v18, 0x3fb8aa3b, v75
	v_exp_f32_e32 v77, v18
	v_div_scale_f32 v18, s[0:1], v82, v82, 1.0
	v_rcp_f32_e32 v69, v18
	v_pk_add_f32 v[76:77], v[76:77], -1.0 op_sel_hi:[1,0]
	v_cmp_lt_f32_e32 vcc, 0, v75
	v_cvt_f32_f16_e32 v80, v70
	v_cvt_f32_f16_sdwa v81, v70 dst_sel:DWORD dst_unused:UNUSED_PAD src0_sel:WORD_1
	v_cndmask_b32_e32 v75, v77, v75, vcc
	v_fma_f32 v77, -v18, v69, 1.0
	v_fmac_f32_e32 v69, v77, v69
	v_div_scale_f32 v77, vcc, 1.0, v82, 1.0
	v_mul_f32_e32 v78, v77, v69
	v_fma_f32 v79, -v18, v78, v77
	v_fmac_f32_e32 v78, v79, v69
	v_fma_f32 v18, -v18, v78, v77
	v_div_fmas_f32 v18, v18, v69, v78
	v_cvt_f32_f16_e32 v78, v58
	v_cvt_f32_f16_sdwa v79, v58 dst_sel:DWORD dst_unused:UNUSED_PAD src0_sel:WORD_1
	s_waitcnt vmcnt(1)
	v_cvt_f32_f16_e32 v84, v62
	v_cvt_f32_f16_sdwa v85, v62 dst_sel:DWORD dst_unused:UNUSED_PAD src0_sel:WORD_1
	v_div_fixup_f32 v18, v18, v82, 1.0
	v_cmp_lt_f32_e32 vcc, 0, v82
	v_pk_add_f32 v[78:79], v[78:79], v[80:81]
	v_cvt_f32_f16_e32 v70, v71
	v_cndmask_b32_e32 v18, 0, v18, vcc
	v_pk_fma_f32 v[78:79], v[102:103], v[84:85], v[78:79] op_sel_hi:[0,1,1]
	v_pk_mul_f32 v[78:79], v[18:19], v[78:79] op_sel_hi:[0,1]
	v_mul_f32_e32 v58, 0x3fb8aa3b, v78
	v_exp_f32_e32 v80, v58
	v_mul_f32_e32 v58, 0x3fb8aa3b, v79
	v_exp_f32_e32 v81, v58
	v_cmp_lt_f32_e32 vcc, 0, v74
	v_cvt_f32_f16_sdwa v71, v71 dst_sel:DWORD dst_unused:UNUSED_PAD src0_sel:WORD_1
	v_cvt_f32_f16_e32 v62, v63
	v_cndmask_b32_e32 v58, v76, v74, vcc
	v_cvt_pk_f16_f32 v69, v58, v75
	v_cvt_f32_f16_e32 v58, v59
	v_cvt_f32_f16_sdwa v59, v59 dst_sel:DWORD dst_unused:UNUSED_PAD src0_sel:WORD_1
	v_cvt_f32_f16_sdwa v63, v63 dst_sel:DWORD dst_unused:UNUSED_PAD src0_sel:WORD_1
	v_pk_add_f32 v[74:75], v[80:81], -1.0 op_sel_hi:[1,0]
	v_cmp_lt_f32_e32 vcc, 0, v79
	v_pk_add_f32 v[58:59], v[58:59], v[70:71]
	v_cvt_f32_f16_sdwa v71, v60 dst_sel:DWORD dst_unused:UNUSED_PAD src0_sel:WORD_1
	v_cndmask_b32_e32 v75, v75, v79, vcc
	v_cmp_lt_f32_e32 vcc, 0, v78
	v_pk_fma_f32 v[58:59], v[102:103], v[62:63], v[58:59] op_sel_hi:[0,1,1]
	v_pk_mul_f32 v[58:59], v[18:19], v[58:59] op_sel_hi:[0,1]
	v_cndmask_b32_e32 v70, v74, v78, vcc
	v_cvt_pk_f16_f32 v94, v70, v75
	v_cvt_f32_f16_e32 v70, v60
	v_cvt_f32_f16_e32 v74, v72
	v_cvt_f32_f16_sdwa v75, v72 dst_sel:DWORD dst_unused:UNUSED_PAD src0_sel:WORD_1
	v_cvt_f32_f16_e32 v76, v64
	v_cvt_f32_f16_sdwa v77, v64 dst_sel:DWORD dst_unused:UNUSED_PAD src0_sel:WORD_1
	v_mul_f32_e32 v62, 0x3fb8aa3b, v58
	v_mul_f32_e32 v63, 0x3fb8aa3b, v59
	v_exp_f32_e32 v62, v62
	v_exp_f32_e32 v63, v63
	v_pk_add_f32 v[70:71], v[70:71], v[74:75]
	v_cmp_lt_f32_e32 vcc, 0, v59
	v_pk_fma_f32 v[70:71], v[102:103], v[76:77], v[70:71] op_sel_hi:[0,1,1]
	v_pk_mul_f32 v[70:71], v[18:19], v[70:71] op_sel_hi:[0,1]
	v_pk_add_f32 v[62:63], v[62:63], -1.0 op_sel_hi:[1,0]
	v_mul_f32_e32 v60, 0x3fb8aa3b, v70
	v_cndmask_b32_e32 v59, v63, v59, vcc
	v_exp_f32_e32 v74, v60
	v_mul_f32_e32 v60, 0x3fb8aa3b, v71
	v_cmp_lt_f32_e32 vcc, 0, v58
	v_exp_f32_e32 v75, v60
	v_cvt_f32_f16_e32 v60, v61
	v_cndmask_b32_e32 v58, v62, v58, vcc
	v_cvt_f32_f16_sdwa v61, v61 dst_sel:DWORD dst_unused:UNUSED_PAD src0_sel:WORD_1
	v_cvt_f32_f16_e32 v62, v73
	v_cvt_f32_f16_sdwa v63, v73 dst_sel:DWORD dst_unused:UNUSED_PAD src0_sel:WORD_1
	v_cvt_f32_f16_e32 v64, v65
	v_cvt_f32_f16_sdwa v65, v65 dst_sel:DWORD dst_unused:UNUSED_PAD src0_sel:WORD_1
	v_cvt_pk_f16_f32 v95, v58, v59
	v_pk_add_f32 v[60:61], v[60:61], v[62:63]
	v_pk_add_f32 v[58:59], v[74:75], -1.0 op_sel_hi:[1,0]
	v_pk_fma_f32 v[60:61], v[102:103], v[64:65], v[60:61] op_sel_hi:[0,1,1]
	v_pk_mul_f32 v[60:61], v[18:19], v[60:61] op_sel_hi:[0,1]
	v_mul_f32_e32 v62, 0x3fb8aa3b, v60
	v_mul_f32_e32 v63, 0x3fb8aa3b, v61
	v_exp_f32_e32 v62, v62
	v_exp_f32_e32 v63, v63
	v_cmp_lt_f32_e32 vcc, 0, v71
	v_cvt_f32_f16_e32 v64, v50
	v_cvt_f32_f16_sdwa v65, v50 dst_sel:DWORD dst_unused:UNUSED_PAD src0_sel:WORD_1
	v_cndmask_b32_e32 v59, v59, v71, vcc
	v_cmp_lt_f32_e32 vcc, 0, v70
	s_waitcnt vmcnt(0)
	v_cvt_f32_f16_sdwa v71, v54 dst_sel:DWORD dst_unused:UNUSED_PAD src0_sel:WORD_1
	s_movk_i32 s0, 0xc4
	v_cndmask_b32_e32 v58, v58, v70, vcc
	v_cvt_pk_f16_f32 v96, v58, v59
	v_pk_add_f32 v[58:59], v[62:63], -1.0 op_sel_hi:[1,0]
	v_cvt_f32_f16_e32 v62, v42
	v_cvt_f32_f16_sdwa v63, v42 dst_sel:DWORD dst_unused:UNUSED_PAD src0_sel:WORD_1
	v_cvt_f32_f16_e32 v70, v54
	v_cmp_lt_f32_e32 vcc, 0, v61
	v_cvt_f32_f16_e32 v54, v55
	v_pk_add_f32 v[62:63], v[62:63], v[64:65]
	v_cndmask_b32_e32 v42, v59, v61, vcc
	v_pk_fma_f32 v[62:63], v[102:103], v[70:71], v[62:63] op_sel_hi:[0,1,1]
	v_pk_mul_f32 v[108:109], v[18:19], v[62:63] op_sel_hi:[0,1]
	v_mul_f32_e32 v50, 0x3fb8aa3b, v108
	v_exp_f32_e32 v62, v50
	v_mul_f32_e32 v50, 0x3fb8aa3b, v109
	v_exp_f32_e32 v63, v50
	v_cmp_lt_f32_e32 vcc, 0, v60
	v_cvt_f32_f16_sdwa v55, v55 dst_sel:DWORD dst_unused:UNUSED_PAD src0_sel:WORD_1
	s_movk_i32 s1, 0x44
	v_cndmask_b32_e32 v50, v58, v60, vcc
	v_pk_add_f32 v[110:111], v[62:63], -1.0 op_sel_hi:[1,0]
	global_load_dwordx4 v[58:61], v106, s[4:5] offset:176
	global_load_dwordx4 v[62:65], v106, s[4:5] offset:160
	global_load_dwordx4 v[70:73], v106, s[4:5] offset:144
	global_load_dwordx4 v[74:77], v106, s[4:5] offset:128
	global_load_dwordx4 v[78:81], v106, s[4:5] offset:112
	global_load_dwordx4 v[82:85], v106, s[4:5] offset:96
	global_load_dwordx4 v[86:89], v106, s[4:5] offset:80
	global_load_dwordx4 v[90:93], v106, s[4:5] offset:64
	v_cvt_pk_f16_f32 v97, v50, v42
	v_cvt_f32_f16_e32 v42, v43
	v_cvt_f32_f16_sdwa v43, v43 dst_sel:DWORD dst_unused:UNUSED_PAD src0_sel:WORD_1
	v_cvt_f32_f16_e32 v50, v51
	v_cvt_f32_f16_sdwa v51, v51 dst_sel:DWORD dst_unused:UNUSED_PAD src0_sel:WORD_1
	v_cmp_lt_f32_e32 vcc, 0, v109
	v_cvt_f32_f16_e32 v106, v52
	v_cvt_f32_f16_e32 v52, v53
	v_cndmask_b32_e32 v103, v111, v109, vcc
	v_pk_add_f32 v[42:43], v[42:43], v[50:51]
	v_cmp_lt_f32_e32 vcc, 0, v108
	v_pk_fma_f32 v[42:43], v[102:103], v[54:55], v[42:43] op_sel_hi:[0,1,1]
	v_cvt_f32_f16_e32 v54, v44
	v_cvt_f32_f16_sdwa v55, v44 dst_sel:DWORD dst_unused:UNUSED_PAD src0_sel:WORD_1
	v_cndmask_b32_e32 v110, v110, v108, vcc
	v_pk_mul_f32 v[42:43], v[18:19], v[42:43] op_sel_hi:[0,1]
	v_cvt_f32_f16_e32 v108, v56
	v_cvt_f32_f16_sdwa v109, v56 dst_sel:DWORD dst_unused:UNUSED_PAD src0_sel:WORD_1
	v_mul_f32_e32 v50, 0x3fb8aa3b, v42
	v_mul_f32_e32 v51, 0x3fb8aa3b, v43
	v_exp_f32_e32 v50, v50
	v_exp_f32_e32 v51, v51
	v_pk_add_f32 v[54:55], v[54:55], v[106:107]
	v_cmp_lt_f32_e32 vcc, 0, v43
	v_pk_fma_f32 v[54:55], v[102:103], v[108:109], v[54:55] op_sel_hi:[0,1,1]
	v_pk_mul_f32 v[54:55], v[18:19], v[54:55] op_sel_hi:[0,1]
	v_pk_add_f32 v[50:51], v[50:51], -1.0 op_sel_hi:[1,0]
	v_mul_f32_e32 v44, 0x3fb8aa3b, v54
	v_cndmask_b32_e32 v43, v51, v43, vcc
	v_exp_f32_e32 v106, v44
	v_mul_f32_e32 v44, 0x3fb8aa3b, v55
	v_cmp_lt_f32_e32 vcc, 0, v42
	v_exp_f32_e32 v107, v44
	v_cvt_f32_f16_sdwa v53, v53 dst_sel:DWORD dst_unused:UNUSED_PAD src0_sel:WORD_1
	v_cndmask_b32_e32 v44, v50, v42, vcc
	v_cvt_pk_f16_f32 v43, v44, v43
	v_cvt_f32_f16_e32 v44, v45
	v_cvt_f32_f16_sdwa v45, v45 dst_sel:DWORD dst_unused:UNUSED_PAD src0_sel:WORD_1
	v_cvt_f32_f16_e32 v56, v57
	v_cvt_f32_f16_sdwa v57, v57 dst_sel:DWORD dst_unused:UNUSED_PAD src0_sel:WORD_1
	v_pk_add_f32 v[50:51], v[106:107], -1.0 op_sel_hi:[1,0]
	v_pk_add_f32 v[44:45], v[44:45], v[52:53]
	v_cmp_lt_f32_e32 vcc, 0, v55
	v_pk_fma_f32 v[44:45], v[102:103], v[56:57], v[44:45] op_sel_hi:[0,1,1]
	v_pk_mul_f32 v[52:53], v[18:19], v[44:45] op_sel_hi:[0,1]
	v_mul_f32_e32 v18, 0x3fb8aa3b, v52
	v_exp_f32_e32 v56, v18
	v_mul_f32_e32 v18, 0x3fb8aa3b, v53
	v_exp_f32_e32 v57, v18
	v_cndmask_b32_e32 v51, v51, v55, vcc
	v_cmp_lt_f32_e32 vcc, 0, v54
	v_cvt_pk_f16_f32 v42, v110, v103
	s_nop 0
	v_cndmask_b32_e32 v18, v50, v54, vcc
	v_cvt_pk_f16_f32 v44, v18, v51
	v_pk_add_f32 v[50:51], v[56:57], -1.0 op_sel_hi:[1,0]
	v_cmp_lt_f32_e32 vcc, 0, v53
	s_nop 1
	v_cndmask_b32_e32 v18, v51, v53, vcc
	v_cmp_lt_f32_e32 vcc, 0, v52
	s_nop 1
	v_cndmask_b32_e32 v45, v50, v52, vcc
	v_cvt_pk_f16_f32 v45, v45, v18
	v_lshrrev_b32_e32 v18, 4, v0
	v_mov_b32_e32 v50, 0x3300
	v_mad_u32_u24 v54, v18, s0, v50
	v_mov_b32_e32 v50, 0x3308
	v_mad_u32_u24 v57, v18, s0, v50
	v_mov_b32_e32 v50, 0x3310
	v_mad_u32_u24 v102, v18, s0, v50
	v_mov_b32_e32 v50, 0x3318
	v_mad_u32_u24 v103, v18, s0, v50
	v_mov_b32_e32 v50, 0x3320
	v_mad_u32_u24 v106, v18, s0, v50
	v_mov_b32_e32 v50, 0x3340
	v_mad_u32_u24 v107, v18, s0, v50
	v_mov_b32_e32 v50, 0x3360
	v_mad_u32_u24 v108, v18, s0, v50
	v_mov_b32_e32 v50, 0x3380
	v_mad_u32_u24 v109, v18, s0, v50
	v_mov_b32_e32 v50, 0x33a0
	v_add_u32_e32 v55, v54, v98
	v_mad_u32_u24 v56, v18, s1, v98
	v_mad_u32_u24 v110, v18, s0, v50
	v_cvt_pk_f16_f32 v19, v19, v20
	v_cvt_pk_f16_f32 v20, v21, v30
	v_cvt_pk_f16_f32 v21, v31, v32
	v_pack_b32_f16 v50, v104, v19
	v_alignbit_b32 v51, v20, v19, 16
	v_alignbit_b32 v52, v21, v20, 16
	v_alignbit_b32 v53, v105, v21, 16
	v_cvt_pk_f16_f32 v19, v27, v28
	v_cvt_pk_f16_f32 v22, v29, v22
	v_mfma_f32_16x16x32_f16 a[0:3], v[34:37], v[50:53], 0
	v_cvt_pk_f16_f32 v23, v23, v24
	v_pack_b32_f16 v20, v26, v19
	v_alignbit_b32 v21, v22, v19, 16
	v_mfma_f32_16x16x32_f16 a[4:7], v[46:49], v[50:53], 0
	v_alignbit_b32 v22, v23, v22, 16
	v_alignbit_b32 v23, v25, v23, 16
	s_cmpk_eq_i32 s2, 0xbf
	v_mfma_f32_16x16x32_f16 a[8:11], v[94:97], v[50:53], 0
	v_mfma_f32_16x16x32_f16 a[0:3], v[38:41], v[20:23], a[0:3]
	s_nop 7
	ds_write_b32 v33, a0
	ds_write_b32 v33, a1 offset:68
	ds_write_b32 v33, a2 offset:136
	v_mfma_f32_16x16x32_f16 a[4:7], v[66:69], v[20:23], a[4:7]
	v_mfma_f32_16x16x32_f16 a[8:11], v[42:45], v[20:23], a[8:11]
	ds_write_b32 v33, a3 offset:204
	s_nop 5
	ds_write_b32 v33, a4 offset:4352
	ds_write_b32 v33, a5 offset:4420
	ds_write_b32 v33, a6 offset:4488
	ds_write_b32 v33, a7 offset:4556
	ds_write_b32 v33, a8 offset:8704
	ds_write_b32 v33, a9 offset:8772
	ds_write_b32 v33, a10 offset:8840
	ds_write_b32 v33, a11 offset:8908
	s_waitcnt lgkmcnt(0)
	s_barrier
	ds_read_b32 v20, v56 offset:8704
	ds_read_b32 v22, v56 offset:9792
	ds_read_b32 v24, v56 offset:10880
	ds_read_b32 v26, v56 offset:11968
	ds_read_b32 v21, v56 offset:4352
	ds_read_b32 v23, v56 offset:5440
	ds_read_b32 v25, v56 offset:6528
	ds_read_b32 v27, v56 offset:7616
	ds_read_b32 v19, v56
	ds_read_b32 v28, v56 offset:1088
	ds_read_b32 v29, v56 offset:2176
	ds_read_b32 v30, v56 offset:3264
	s_waitcnt lgkmcnt(6)
	v_pk_add_f32 v[20:21], v[20:21], v[22:23]
	s_waitcnt lgkmcnt(2)
	v_add_f32_e32 v19, v19, v28
	s_waitcnt lgkmcnt(1)
	v_add_f32_e32 v19, v19, v29
	v_pk_add_f32 v[20:21], v[20:21], v[24:25]
	s_waitcnt lgkmcnt(0)
	v_add_f32_e32 v19, v19, v30
	v_pk_add_f32 v[20:21], v[20:21], v[26:27]
	v_add_f32_e32 v19, v100, v19
	v_mul_f32_e32 v22, 0x3fb8aa3b, v19
	v_pk_add_f32 v[20:21], v[100:101], v[20:21] op_sel_hi:[0,1]
	v_exp_f32_e32 v22, v22
	v_mul_f32_e32 v23, 0x3fb8aa3b, v21
	v_exp_f32_e32 v23, v23
	v_cmp_lt_f32_e32 vcc, 0, v19
	v_add_f32_e32 v22, -1.0, v22
	s_nop 0
	v_cndmask_b32_e32 v19, v22, v19, vcc
	v_add_f32_e32 v22, -1.0, v23
	v_mul_f32_e32 v23, 0x3fb8aa3b, v20
	v_exp_f32_e32 v23, v23
	v_cmp_lt_f32_e32 vcc, 0, v21
	s_nop 1
	v_cndmask_b32_e32 v21, v22, v21, vcc
	ds_write2_b32 v55, v19, v21 offset1:16
	v_add_f32_e32 v19, -1.0, v23
	v_cmp_lt_f32_e32 vcc, 0, v20
	s_nop 1
	v_cndmask_b32_e32 v19, v19, v20, vcc
	ds_write_b32 v55, v19 offset:128
	s_waitcnt lgkmcnt(0)
	s_barrier
	ds_read2_b32 v[20:21], v54 offset1:1
	ds_read2_b32 v[22:23], v57 offset1:1
	ds_read2_b32 v[24:25], v102 offset1:1
	ds_read2_b32 v[26:27], v103 offset1:1
	s_waitcnt lgkmcnt(3)
	v_mul_f32_e32 v19, v21, v15
	v_fmac_f32_e32 v19, v20, v14
	s_waitcnt lgkmcnt(2)
	v_fmac_f32_e32 v19, v22, v16
	s_waitcnt lgkmcnt(1)
	v_mul_f32_e32 v16, v25, v11
	v_fmac_f32_e32 v16, v24, v10
	v_mov_b32_e32 v11, 0x3338
	v_fmac_f32_e32 v19, v23, v17
	s_waitcnt lgkmcnt(0)
	v_fmac_f32_e32 v16, v26, v12
	v_mov_b32_e32 v10, 0x3330
	v_mad_u32_u24 v14, v18, s0, v11
	v_mov_b32_e32 v11, 0x3328
	v_fmac_f32_e32 v16, v27, v13
	v_mad_u32_u24 v10, v18, s0, v10
	v_mad_u32_u24 v12, v18, s0, v11
	v_add_f32_e32 v17, v101, v19
	ds_read2_b32 v[10:11], v10 offset1:1
	ds_read2_b32 v[12:13], v12 offset1:1
	ds_read2_b32 v[14:15], v14 offset1:1
	v_add_f32_e32 v19, v17, v16
	ds_read2_b32 v[16:17], v106 offset1:1
	s_waitcnt lgkmcnt(3)
	v_pk_mul_f32 v[2:3], v[10:11], v[2:3]
	s_waitcnt lgkmcnt(2)
	v_pk_mul_f32 v[8:9], v[12:13], v[8:9]
	s_waitcnt lgkmcnt(1)
	v_pk_mul_f32 v[4:5], v[14:15], v[4:5]
	v_mov_b32_e32 v11, v2
	s_waitcnt lgkmcnt(0)
	v_pk_mul_f32 v[6:7], v[16:17], v[6:7]
	ds_read2_b32 v[12:13], v107 offset1:1
	ds_read2_b32 v[14:15], v108 offset1:1
	ds_read2_b32 v[20:21], v109 offset1:1
	v_mov_b32_e32 v10, v6
	v_mov_b32_e32 v2, v7
	v_pk_add_f32 v[2:3], v[10:11], v[2:3]
	v_mov_b32_e32 v6, v8
	v_mov_b32_e32 v7, v4
	v_pk_add_f32 v[2:3], v[2:3], v[6:7]
	v_mov_b32_e32 v4, v9
	v_pk_add_f32 v[2:3], v[2:3], v[4:5]
	v_mov_b32_e32 v4, 0x3350
	v_mad_u32_u24 v10, v18, s0, v4
	v_mov_b32_e32 v4, 0x3358
	v_mad_u32_u24 v6, v18, s0, v4
	v_mov_b32_e32 v4, 0x3348
	v_mov_b32_e32 v5, 0x3370
	v_mad_u32_u24 v4, v18, s0, v4
	v_mad_u32_u24 v8, v18, s0, v5
	ds_read2_b32 v[16:17], v110 offset1:1
	ds_read2_b32 v[4:5], v4 offset1:1
	ds_read2_b32 v[6:7], v6 offset1:1
	ds_read2_b32 v[8:9], v8 offset1:1
	ds_read2_b32 v[10:11], v10 offset1:1
	v_add_f32_e32 v2, v19, v2
	v_add_f32_e32 v19, v2, v3
	s_waitcnt vmcnt(0) lgkmcnt(3)
	v_pk_mul_f32 v[2:3], v[4:5], v[92:93]
	s_waitcnt lgkmcnt(2)
	v_pk_mul_f32 v[4:5], v[6:7], v[88:89]
	v_pk_mul_f32 v[6:7], v[12:13], v[90:91]
	s_waitcnt lgkmcnt(0)
	v_pk_mul_f32 v[10:11], v[10:11], v[86:87]
	v_mov_b32_e32 v12, v6
	v_mov_b32_e32 v13, v10
	v_mov_b32_e32 v10, v7
	v_pk_add_f32 v[6:7], v[12:13], v[10:11]
	v_mov_b32_e32 v10, v2
	v_mov_b32_e32 v11, v4
	v_pk_add_f32 v[6:7], v[6:7], v[10:11]
	v_mov_b32_e32 v4, v3
	v_pk_add_f32 v[2:3], v[6:7], v[4:5]
	v_pk_mul_f32 v[12:13], v[14:15], v[82:83]
	v_add_f32_e32 v2, v19, v2
	v_add_f32_e32 v19, v2, v3
	v_mov_b32_e32 v2, 0x3378
	v_mov_b32_e32 v3, 0x3368
	v_mad_u32_u24 v2, v18, s0, v2
	v_mad_u32_u24 v4, v18, s0, v3
	ds_read2_b32 v[2:3], v2 offset1:1
	ds_read2_b32 v[4:5], v4 offset1:1
	v_pk_mul_f32 v[8:9], v[8:9], v[78:79]
	v_mov_b32_e32 v14, v12
	v_mov_b32_e32 v15, v8
	s_waitcnt lgkmcnt(1)
	v_pk_mul_f32 v[2:3], v[2:3], v[80:81]
	s_waitcnt lgkmcnt(0)
	v_pk_mul_f32 v[4:5], v[4:5], v[84:85]
	v_mov_b32_e32 v8, v13
	v_pk_add_f32 v[8:9], v[14:15], v[8:9]
	v_mov_b32_e32 v12, v4
	v_mov_b32_e32 v13, v2
	v_pk_add_f32 v[8:9], v[8:9], v[12:13]
	v_mov_b32_e32 v2, v5
	v_pk_add_f32 v[2:3], v[8:9], v[2:3]
	v_mov_b32_e32 v6, 0x3390
	v_add_f32_e32 v2, v19, v2
	v_mov_b32_e32 v7, 0x3398
	v_add_f32_e32 v19, v2, v3
	v_mov_b32_e32 v2, 0x3388
	v_mad_u32_u24 v6, v18, s0, v6
	v_mad_u32_u24 v10, v18, s0, v7
	v_mad_u32_u24 v2, v18, s0, v2
	ds_read2_b32 v[6:7], v6 offset1:1
	ds_read2_b32 v[10:11], v10 offset1:1
	ds_read2_b32 v[2:3], v2 offset1:1
	v_mov_b32_e32 v5, 0x33b8
	v_mov_b32_e32 v4, 0x33b0
	v_mad_u32_u24 v8, v18, s0, v5
	v_mov_b32_e32 v5, 0x33a8
	v_mad_u32_u24 v4, v18, s0, v4
	v_mad_u32_u24 v12, v18, s0, v5
	v_pk_mul_f32 v[14:15], v[20:21], v[74:75]
	s_waitcnt lgkmcnt(2)
	v_pk_mul_f32 v[6:7], v[6:7], v[70:71]
	ds_read2_b32 v[4:5], v4 offset1:1
	ds_read2_b32 v[8:9], v8 offset1:1
	ds_read2_b32 v[12:13], v12 offset1:1
	s_waitcnt lgkmcnt(3)
	v_pk_mul_f32 v[2:3], v[2:3], v[76:77]
	v_pk_mul_f32 v[10:11], v[10:11], v[72:73]
	v_mov_b32_e32 v20, v14
	v_mov_b32_e32 v21, v6
	v_mov_b32_e32 v6, v15
	v_pk_add_f32 v[6:7], v[20:21], v[6:7]
	v_mov_b32_e32 v14, v2
	v_mov_b32_e32 v15, v10
	v_pk_add_f32 v[6:7], v[6:7], v[14:15]
	v_mov_b32_e32 v10, v3
	v_pk_add_f32 v[2:3], v[6:7], v[10:11]
	s_waitcnt lgkmcnt(1)
	v_pk_mul_f32 v[6:7], v[8:9], v[60:61]
	v_add_f32_e32 v2, v19, v2
	v_pk_mul_f32 v[8:9], v[16:17], v[62:63]
	v_pk_mul_f32 v[4:5], v[4:5], v[58:59]
	v_add_f32_e32 v14, v2, v3
	s_waitcnt lgkmcnt(0)
	v_pk_mul_f32 v[2:3], v[12:13], v[64:65]
	v_mov_b32_e32 v10, v8
	v_mov_b32_e32 v11, v4
	v_mov_b32_e32 v4, v9
	v_pk_add_f32 v[4:5], v[10:11], v[4:5]
	v_mov_b32_e32 v8, v2
	v_mov_b32_e32 v9, v6
	v_pk_add_f32 v[4:5], v[4:5], v[8:9]
	v_mov_b32_e32 v6, v3
	v_pk_add_f32 v[2:3], v[4:5], v[6:7]
	s_mov_b32 s0, 0x800000
	v_add_f32_e32 v2, v14, v2
	v_add_f32_e32 v8, v2, v3
	v_mbcnt_lo_u32_b32 v2, -1, 0
	v_mbcnt_hi_u32_b32 v2, -1, v2
	v_and_b32_e32 v3, 64, v2
	v_add_u32_e32 v4, 64, v3
	v_xor_b32_e32 v3, 8, v2
	v_cmp_lt_i32_e32 vcc, v3, v4
	s_nop 1
	v_cndmask_b32_e32 v3, v2, v3, vcc
	v_lshlrev_b32_e32 v3, 2, v3
	ds_bpermute_b32 v5, v3, v8
	s_waitcnt lgkmcnt(0)
	v_max_f32_e32 v5, v5, v5
	v_max_f32_e32 v6, v8, v5
	v_xor_b32_e32 v5, 4, v2
	v_cmp_lt_i32_e32 vcc, v5, v4
	s_nop 1
	v_cndmask_b32_e32 v5, v2, v5, vcc
	v_lshlrev_b32_e32 v5, 2, v5
	ds_bpermute_b32 v7, v5, v6
	s_waitcnt lgkmcnt(0)
	v_max_f32_e32 v7, v7, v7
	v_max_f32_e32 v7, v6, v7
	v_xor_b32_e32 v6, 2, v2
	v_cmp_lt_i32_e32 vcc, v6, v4
	s_nop 1
	v_cndmask_b32_e32 v6, v2, v6, vcc
	v_lshlrev_b32_e32 v6, 2, v6
	ds_bpermute_b32 v9, v6, v7
	s_waitcnt lgkmcnt(0)
	v_max_f32_e32 v9, v9, v9
	v_max_f32_e32 v9, v7, v9
	v_xor_b32_e32 v7, 1, v2
	v_cmp_lt_i32_e32 vcc, v7, v4
	s_nop 1
	v_cndmask_b32_e32 v7, v2, v7, vcc
	v_lshlrev_b32_e32 v7, 2, v7
	ds_bpermute_b32 v10, v7, v9
	s_waitcnt lgkmcnt(0)
	v_max_f32_e32 v10, v10, v10
	v_max_f32_e32 v9, v9, v10
	v_sub_f32_e32 v8, v8, v9
	v_mul_f32_e32 v9, 0x3fb8aa3b, v8
	v_exp_f32_e32 v9, v9
	ds_bpermute_b32 v10, v3, v9
	s_waitcnt lgkmcnt(0)
	v_add_f32_e32 v9, v9, v10
	ds_bpermute_b32 v10, v5, v9
	s_waitcnt lgkmcnt(0)
	v_add_f32_e32 v9, v9, v10
	ds_bpermute_b32 v10, v6, v9
	s_waitcnt lgkmcnt(0)
	v_add_f32_e32 v9, v9, v10
	ds_bpermute_b32 v10, v7, v9
	s_waitcnt lgkmcnt(0)
	v_add_f32_e32 v9, v9, v10
	v_cmp_gt_f32_e32 vcc, s0, v9
	s_mov_b32 s0, 0x3f317217
	s_nop 0
	v_cndmask_b32_e64 v10, 0, 32, vcc
	v_ldexp_f32 v9, v9, v10
	v_log_f32_e32 v9, v9
	s_nop 0
	v_mul_f32_e32 v10, 0x3f317217, v9
	v_fma_f32 v10, v9, s0, -v10
	v_fmamk_f32 v10, v9, 0x3377d1cf, v10
	s_mov_b32 s0, 0x7f800000
	v_fmac_f32_e32 v10, 0x3f317217, v9
	v_cmp_lt_f32_e64 s[0:1], |v9|, s0
	s_nop 1
	v_cndmask_b32_e64 v9, v9, v10, s[0:1]
	v_mov_b32_e32 v10, 0x41b17218
	v_cndmask_b32_e32 v10, 0, v10, vcc
	v_sub_f32_e32 v9, v9, v10
	v_sub_f32_e32 v10, v8, v9
	v_or_b32_e32 v8, s3, v18
	v_ashrrev_i32_e32 v9, 31, v8
	v_lshlrev_b64 v[8:9], 6, v[8:9]
	v_lshl_add_u64 v[8:9], s[8:9], 0, v[8:9]
	s_cselect_b64 s[0:1], -1, 0
	v_cmp_eq_u32_e32 vcc, 3, v1
	v_lshl_add_u64 v[8:9], v[8:9], 0, v[98:99]
	s_and_b64 s[0:1], s[0:1], vcc
	global_store_dword v[8:9], v10, off

	.amdhsa_kernel _Z10epi_kernelPKDF16_PKfS2_S2_S2_S2_Pf
		.amdhsa_group_segment_fixed_size 16192
		.amdhsa_private_segment_fixed_size 0
		.amdhsa_kernarg_size 56
		.amdhsa_user_sgpr_count 2
		.amdhsa_user_sgpr_dispatch_ptr 0
		.amdhsa_user_sgpr_queue_ptr 0
		.amdhsa_user_sgpr_kernarg_segment_ptr 1
		.amdhsa_user_sgpr_dispatch_id 0
		.amdhsa_user_sgpr_kernarg_preload_length 0
		.amdhsa_user_sgpr_kernarg_preload_offset 0
		.amdhsa_user_sgpr_private_segment_size 0
		.amdhsa_uses_dynamic_stack 0
		.amdhsa_enable_private_segment 0
		.amdhsa_system_sgpr_workgroup_id_x 1
		.amdhsa_system_sgpr_workgroup_id_y 0
		.amdhsa_system_sgpr_workgroup_id_z 0
		.amdhsa_system_sgpr_workgroup_info 0
		.amdhsa_system_vgpr_workitem_id 0
		.amdhsa_next_free_vgpr 140
		.amdhsa_next_free_sgpr 32
		.amdhsa_accum_offset 128
		.amdhsa_reserve_vcc 1
		.amdhsa_float_round_mode_32 0
		.amdhsa_float_round_mode_16_64 0
		.amdhsa_float_denorm_mode_32 3
		.amdhsa_float_denorm_mode_16_64 3
		.amdhsa_dx10_clamp 1
		.amdhsa_ieee_mode 1
		.amdhsa_fp16_overflow 0
		.amdhsa_tg_split 0
		.amdhsa_exception_fp_ieee_invalid_op 0
		.amdhsa_exception_fp_denorm_src 0
		.amdhsa_exception_fp_ieee_div_zero 0
		.amdhsa_exception_fp_ieee_overflow 0
		.amdhsa_exception_fp_ieee_underflow 0
		.amdhsa_exception_fp_ieee_inexact 0
		.amdhsa_exception_int_div_zero 0
	.end_amdhsa_kernel

amdhsa.kernels:
  - .agpr_count:     0
    .args:
      - .actual_access:  read_only
        .address_space:  global
        .offset:         0
        .size:           8
        .value_kind:     global_buffer
      - .actual_access:  read_only
        .address_space:  global
        .offset:         8
        .size:           8
        .value_kind:     global_buffer
      - .actual_access:  read_only
        .address_space:  global
        .offset:         16
        .size:           8
        .value_kind:     global_buffer
      - .actual_access:  write_only
        .address_space:  global
        .offset:         24
        .size:           8
        .value_kind:     global_buffer
      - .actual_access:  write_only
        .address_space:  global
        .offset:         32
        .size:           8
        .value_kind:     global_buffer
      - .actual_access:  write_only
        .address_space:  global
        .offset:         40
        .size:           8
        .value_kind:     global_buffer
    .group_segment_fixed_size: 57344
    .kernarg_segment_align: 8
    .kernarg_segment_size: 48
    .language:       OpenCL C
    .language_version:
      - 2
      - 0
    .max_flat_workgroup_size: 512
    .name:           _Z12gemm1_kernelPKfS0_S0_PDv8_DF16_PDF16_S3_
    .private_segment_fixed_size: 0
    .sgpr_count:     18
    .sgpr_spill_count: 0
    .symbol:         _Z12gemm1_kernelPKfS0_S0_PDv8_DF16_PDF16_S3_.kd
    .uniform_work_group_size: 1
    .uses_dynamic_stack: false
    .vgpr_count:     125
    .vgpr_spill_count: 0
    .wavefront_size: 64
  - .agpr_count:     0
    .args:
      - .actual_access:  read_only
        .address_space:  global
        .offset:         0
        .size:           8
        .value_kind:     global_buffer
      - .actual_access:  read_only
        .address_space:  global
        .offset:         8
        .size:           8
        .value_kind:     global_buffer
      - .actual_access:  read_only
        .address_space:  global
        .offset:         16
        .size:           8
        .value_kind:     global_buffer
      - .actual_access:  read_only
        .address_space:  global
        .offset:         24
        .size:           8
        .value_kind:     global_buffer
      - .actual_access:  write_only
        .address_space:  global
        .offset:         32
        .size:           8
        .value_kind:     global_buffer
      - .actual_access:  write_only
        .address_space:  global
        .offset:         40
        .size:           8
        .value_kind:     global_buffer
    .group_segment_fixed_size: 160768
    .kernarg_segment_align: 8
    .kernarg_segment_size: 48
    .language:       OpenCL C
    .language_version:
      - 2
      - 0
    .max_flat_workgroup_size: 768
    .name:           _Z11attn_kernelPKiPKDv8_DF16_PKDF16_S5_PDF16_Pf
    .private_segment_fixed_size: 0
    .sgpr_count:     55
    .sgpr_spill_count: 0
    .symbol:         _Z11attn_kernelPKiPKDv8_DF16_PKDF16_S5_PDF16_Pf.kd
    .uniform_work_group_size: 1
    .uses_dynamic_stack: false
    .vgpr_count:     168
    .vgpr_spill_count: 0
    .wavefront_size: 64
  - .agpr_count:     12
    .args:
      - .actual_access:  read_only
        .address_space:  global
        .offset:         0
        .size:           8
        .value_kind:     global_buffer
      - .actual_access:  read_only
        .address_space:  global
        .offset:         8
        .size:           8
        .value_kind:     global_buffer
      - .actual_access:  read_only
        .address_space:  global
        .offset:         16
        .size:           8
        .value_kind:     global_buffer
      - .actual_access:  read_only
        .address_space:  global
        .offset:         24
        .size:           8
        .value_kind:     global_buffer
      - .actual_access:  read_only
        .address_space:  global
        .offset:         32
        .size:           8
        .value_kind:     global_buffer
      - .actual_access:  read_only
        .address_space:  global
        .offset:         40
        .size:           8
        .value_kind:     global_buffer
      - .actual_access:  write_only
        .address_space:  global
        .offset:         48
        .size:           8
        .value_kind:     global_buffer
    .group_segment_fixed_size: 16192
    .kernarg_segment_align: 8
    .kernarg_segment_size: 56
    .language:       OpenCL C
    .language_version:
      - 2
      - 0
    .max_flat_workgroup_size: 256
    .name:           _Z10epi_kernelPKDF16_PKfS2_S2_S2_S2_Pf
    .private_segment_fixed_size: 0
    .sgpr_count:     38
    .sgpr_spill_count: 0
    .symbol:         _Z10epi_kernelPKDF16_PKfS2_S2_S2_S2_Pf.kd
    .uniform_work_group_size: 1
    .uses_dynamic_stack: false
    .vgpr_count:     140
    .vgpr_spill_count: 0
    .wavefront_size: 64
